# in-proj K-loop load segments without VALU: LDS-DMA in saddr form with SGPR pointer arithmetic, one precomputed VGPR base for B-fragment reads; on top of v33
# baseline (speedup 1.0000x reference)
;     __device__ __forceinline__ void a_ready(const Unit&) const { if (++ncall == 3 && sig != nullptr && threadIdx.x == 0) __hip_atomic_fetch_add(sig, 1u, __ATOMIC_RELAXED, __HIP_MEMORY_SCOPE_AGENT); }
;     __device__ bool next(int i, Unit& u) const { if (!base.next(i >> 1, u)) return false; if (i & 1) { u.pm += MTOK / BM; u.pn += DM / BM; } return true; }
; #define PG8_STAGE(bufoff, gbase, voff) do { _Pragma("unroll") for (int _i = 0; _i < 2; ++_i) \
;         __builtin_amdgcn_global_load_lds((const unsigned*)((const char*)(gbase) + (voff)[_i]), (PG8_LAS unsigned*)(lds + (bufoff) + ldsw + _i * 8192), 16, 0, 0); } while (0)
; #define PG8_LDA(dst, b, h) do { _Pragma("unroll") for (int m = 0; m < 4; ++m) _Pragma("unroll") for (int k = 0; k < 2; ++k) dst[m][k] = *(const PG8_LAS bf16x8*)(lds + PG8_SA(b, h) + aoff + m * 2048 + k * 1024); } while (0)
; #define PG8_LDB(dst, b, h) do { _Pragma("unroll") for (int n = 0; n < 2; ++n) _Pragma("unroll") for (int k = 0; k < 2; ++k) dst[n][k] = *(const PG8_LAS bf16x8*)(lds + PG8_SB(b, h) + boff + n * 2048 + k * 1024); } while (0)
; #define PG8_SCHED __builtin_amdgcn_sched_barrier(0)
;   __device__ __forceinline__ bool next(int i,AttnUnit&u)const{ if(i>=2||vcu>=256)return false; const int s=vcu&3; u.bh=vcu>>2; u.qb=(i==0)?7-s:s; return true; }
; template <class Epi, class Sched, bool ALIGN_EPI = false, bool SP2 = false>
; __device__ __forceinline__ void gemm_phase(PG8_LAS unsigned char* lds, const Gemm g, const Sched& S, const Epi& E) {
;     ...
;         const bool has_next = S.next(ui + 1, nxt);
;         const char* nA = has_next ? (const char*)g.A + (size_t)nxt.pm * tstep + (nxt.half == 2 ? hstep : (size_t)0) : cA; const char* nB = has_next ? (const char*)g.Bt + (size_t)nxt.pn * tstep : cB;
;         for (int t = 0; t < nt; t += 2) {
;             const bool last = (t == nt - 2);
;             const char* a1 = cA + (size_t)(t + 1) * kstep;
;             const char* a2 = last ? nA : cA + (size_t)(t + 2) * kstep; const char* b2 = last ? nB : cB + (size_t)(t + 2) * kstep;
;             const char* a3 = a2 + kstep; const char* b3 = b2 + kstep;
;             if (last && has_next) S.a_ready(nxt);
;             if constexpr (SP2) {
;             PG8_LDB(B0, 0, 0); PG8_LDB(B1, 0, 1); PG8_SCHED; PG8_LDA(At, 0, 0); PG8_STAGE(PG8_SA(1, 1), a1 + hstep, voffA);
.LBB0_394:
	s_ashr_i32 s61, s60, 31
	s_lshl_b64 s[10:11], s[60:61], 19
	s_add_u32 s66, s24, s10
	s_addc_u32 s67, s25, s11
	s_and_b64 s[10:11], s[64:65], exec
	s_cselect_b32 s12, s67, s9
	s_cselect_b32 s13, s66, s8
	s_ashr_i32 s63, s62, 31
	s_lshl_b64 s[10:11], s[62:63], 19
	s_add_u32 s68, s28, s10
	s_addc_u32 s69, s29, s11
	s_and_b64 s[10:11], s[64:65], exec
	s_cselect_b32 s14, s69, s1
	s_cselect_b32 s15, s68, s0
	s_add_u32 s8, s8, 0x40080
	s_addc_u32 s9, s9, 0
	s_add_u32 s36, s0, 0x100
	s_addc_u32 s38, s1, 0
	s_mov_b32 s39, -2
	s_waitcnt lgkmcnt(0)
	v_add_u32_e32 v238, 0x10000, v203
	s_add_u32 s0, s8, 0xfffc0080
	s_addc_u32 s1, s9, -1
	s_cmp_eq_u32 s39, 12
	s_cselect_b32 s11, s12, s1
	s_cselect_b32 s10, s13, s0
	s_cselect_b32 s1, s14, s38
	s_cselect_b32 s0, s15, s36
	ds_read_b128 v[132:135], v238
	ds_read_b128 v[136:139], v238 offset:1024
	ds_read_b128 v[140:143], v238 offset:2048
	ds_read_b128 v[144:147], v238 offset:3072
	ds_read_b128 v[148:151], v238 offset:16384
	ds_read_b128 v[152:155], v238 offset:17408
	ds_read_b128 v[156:159], v238 offset:18432
	ds_read_b128 v[160:163], v238 offset:19456
	s_add_i32 m0, s19, 0xc000
	ds_read_b128 v[182:185], v206
	ds_read_b128 v[186:189], v206 offset:1024
	ds_read_b128 v[190:193], v206 offset:2048
	ds_read_b128 v[194:197], v206 offset:3072
	global_load_lds_dwordx4 v164, s[8:9]
	s_add_i32 m0, s19, 0xe000
	ds_read_b128 v[198:201], v206 offset:4096
	ds_read_b128 v[208:211], v206 offset:5120
	ds_read_b128 v[212:215], v206 offset:6144
	ds_read_b128 v[216:219], v206 offset:7168
	global_load_lds_dwordx4 v168, s[8:9]
	s_cmp_eq_u32 s32, 0
	s_cbranch_scc1 .Lpw_ip_1
	s_waitcnt vmcnt(24)
	s_branch .Lpj_ip_1

; #define PG8_STAGE(bufoff, gbase, voff) do { _Pragma("unroll") for (int _i = 0; _i < 2; ++_i) \
;         __builtin_amdgcn_global_load_lds((const unsigned*)((const char*)(gbase) + (voff)[_i]), (PG8_LAS unsigned*)(lds + (bufoff) + ldsw + _i * 8192), 16, 0, 0); } while (0)
; #define PG8_LDA(dst, b, h) do { _Pragma("unroll") for (int m = 0; m < 4; ++m) _Pragma("unroll") for (int k = 0; k < 2; ++k) dst[m][k] = *(const PG8_LAS bf16x8*)(lds + PG8_SA(b, h) + aoff + m * 2048 + k * 1024); } while (0)
; #define PG8_MMA(ai, bj, At, Bt) do { __builtin_amdgcn_s_setprio(1); _Pragma("unroll") for (int m = 0; m < 4; ++m) _Pragma("unroll") for (int n = 0; n < 2; ++n) _Pragma("unroll") for (int k = 0; k < 2; ++k) \
;         acc[ai][bj][m][n] = __builtin_amdgcn_mfma_f32_16x16x32_bf16(Bt[n][k], At[m][k], acc[ai][bj][m][n], 0, 0, 0); __builtin_amdgcn_s_setprio(0); } while (0)
; #define PG8_WAIT_V(n) asm volatile("s_waitcnt vmcnt(" #n ")" ::: "memory")
; #define PG8_WAIT_L(n) asm volatile("s_waitcnt lgkmcnt(" #n ")" ::: "memory")
; #define PG8_BAR __builtin_amdgcn_s_barrier()
; #define PG8_SCHED __builtin_amdgcn_sched_barrier(0)
; template <class Epi, class Sched, bool ALIGN_EPI = false, bool SP2 = false>
; __device__ __forceinline__ void gemm_phase(PG8_LAS unsigned char* lds, const Gemm g, const Sched& S, const Epi& E) {
;     ...
;             PG8_WAIT_V(8); PG8_WAIT_L(0); PG8_BAR; PG8_MMA(0, 0, At, B0); PG8_MMA(0, 1, At, B1); PG8_BAR; PG8_SCHED;
;             PG8_LDA(At, 0, 1); PG8_STAGE(PG8_SB(0, 0), b2, voffB); PG8_STAGE(PG8_SB(0, 1), b2 + hstep, voffB); PG8_STAGE(PG8_SA(0, 0), a2, voffA);
;             PG8_WAIT_V(8); PG8_WAIT_L(0); PG8_BAR; if (cur.half == 0) { PG8_MMA(1, 0, At, B0); PG8_MMA(1, 1, At, B1); } PG8_BAR; PG8_SCHED;
.Lpj_ip_1:
	s_waitcnt lgkmcnt(0)
	s_barrier
	s_setprio 1
	s_waitcnt lgkmcnt(0)
	v_mfma_f32_16x16x32_bf16 v[128:131], v[132:135], v[182:185], 0
	v_mfma_f32_16x16x32_bf16 v[124:127], v[140:143], v[182:185], 0
	v_mfma_f32_16x16x32_bf16 v[112:115], v[132:135], v[190:193], 0
	v_mfma_f32_16x16x32_bf16 v[108:111], v[140:143], v[190:193], 0
	v_mfma_f32_16x16x32_bf16 v[96:99], v[132:135], v[198:201], 0
	v_mfma_f32_16x16x32_bf16 v[92:95], v[140:143], v[198:201], 0
	v_mfma_f32_16x16x32_bf16 v[80:83], v[132:135], v[212:215], 0
	v_mfma_f32_16x16x32_bf16 v[76:79], v[140:143], v[212:215], 0
	v_mfma_f32_16x16x32_bf16 v[128:131], v[136:139], v[186:189], v[128:131]
	v_mfma_f32_16x16x32_bf16 v[124:127], v[144:147], v[186:189], v[124:127]
	v_mfma_f32_16x16x32_bf16 v[112:115], v[136:139], v[194:197], v[112:115]
	v_mfma_f32_16x16x32_bf16 v[108:111], v[144:147], v[194:197], v[108:111]
	v_mfma_f32_16x16x32_bf16 v[96:99], v[136:139], v[208:211], v[96:99]
	v_mfma_f32_16x16x32_bf16 v[92:95], v[144:147], v[208:211], v[92:95]
	v_mfma_f32_16x16x32_bf16 v[80:83], v[136:139], v[216:219], v[80:83]
	v_mfma_f32_16x16x32_bf16 v[76:79], v[144:147], v[216:219], v[76:79]
	s_setprio 0
	s_setprio 1
	v_mfma_f32_16x16x32_bf16 v[120:123], v[148:151], v[182:185], 0
	v_mfma_f32_16x16x32_bf16 v[116:119], v[156:159], v[182:185], 0
	v_mfma_f32_16x16x32_bf16 v[104:107], v[148:151], v[190:193], 0
	v_mfma_f32_16x16x32_bf16 v[100:103], v[156:159], v[190:193], 0
	v_mfma_f32_16x16x32_bf16 v[88:91], v[148:151], v[198:201], 0
	v_mfma_f32_16x16x32_bf16 v[84:87], v[156:159], v[198:201], 0
	v_mfma_f32_16x16x32_bf16 v[72:75], v[148:151], v[212:215], 0
	v_mfma_f32_16x16x32_bf16 v[68:71], v[156:159], v[212:215], 0
	v_mfma_f32_16x16x32_bf16 v[120:123], v[152:155], v[186:189], v[120:123]
	v_mfma_f32_16x16x32_bf16 v[116:119], v[160:163], v[186:189], v[116:119]
	v_mfma_f32_16x16x32_bf16 v[104:107], v[152:155], v[194:197], v[104:107]
	v_mfma_f32_16x16x32_bf16 v[100:103], v[160:163], v[194:197], v[100:103]
	v_mfma_f32_16x16x32_bf16 v[88:91], v[152:155], v[208:211], v[88:91]
	v_mfma_f32_16x16x32_bf16 v[84:87], v[160:163], v[208:211], v[84:87]
	v_mfma_f32_16x16x32_bf16 v[72:75], v[152:155], v[216:219], v[72:75]
	v_mfma_f32_16x16x32_bf16 v[68:71], v[160:163], v[216:219], v[68:71]
	s_setprio 0
	s_barrier
	s_add_i32 m0, s19, 0x10000
	ds_read_b128 v[182:185], v206 offset:16384
	ds_read_b128 v[186:189], v206 offset:17408
	global_load_lds_dwordx4 v166, s[0:1]
	s_add_i32 m0, s19, 0x12000
	s_add_u32 s78, s0, 0x40000
	s_addc_u32 s79, s1, 0
	ds_read_b128 v[190:193], v206 offset:18432
	ds_read_b128 v[194:197], v206 offset:19456
	global_load_lds_dwordx4 v170, s[0:1]
	s_add_i32 m0, s19, 0x14000
	ds_read_b128 v[198:201], v206 offset:20480
	ds_read_b128 v[208:211], v206 offset:21504
	global_load_lds_dwordx4 v166, s[78:79]
	s_add_i32 m0, s19, 0x16000
	ds_read_b128 v[212:215], v206 offset:22528
	ds_read_b128 v[216:219], v206 offset:23552
	global_load_lds_dwordx4 v170, s[78:79]
	s_mov_b32 m0, s19
	s_nop 0
	global_load_lds_dwordx4 v164, s[10:11]
	s_mov_b32 m0, s30
	s_nop 0
	global_load_lds_dwordx4 v168, s[10:11]
	s_cmp_eq_u32 s32, 0
	s_cbranch_scc1 .Lpw_ip_2
	s_waitcnt vmcnt(24)
	s_branch .Lpj_ip_2

; #define PG8_STAGE(bufoff, gbase, voff) do { _Pragma("unroll") for (int _i = 0; _i < 2; ++_i) \
;         __builtin_amdgcn_global_load_lds((const unsigned*)((const char*)(gbase) + (voff)[_i]), (PG8_LAS unsigned*)(lds + (bufoff) + ldsw + _i * 8192), 16, 0, 0); } while (0)
; #define PG8_LDA(dst, b, h) do { _Pragma("unroll") for (int m = 0; m < 4; ++m) _Pragma("unroll") for (int k = 0; k < 2; ++k) dst[m][k] = *(const PG8_LAS bf16x8*)(lds + PG8_SA(b, h) + aoff + m * 2048 + k * 1024); } while (0)
; #define PG8_LDB(dst, b, h) do { _Pragma("unroll") for (int n = 0; n < 2; ++n) _Pragma("unroll") for (int k = 0; k < 2; ++k) dst[n][k] = *(const PG8_LAS bf16x8*)(lds + PG8_SB(b, h) + boff + n * 2048 + k * 1024); } while (0)
; #define PG8_MMA(ai, bj, At, Bt) do { __builtin_amdgcn_s_setprio(1); _Pragma("unroll") for (int m = 0; m < 4; ++m) _Pragma("unroll") for (int n = 0; n < 2; ++n) _Pragma("unroll") for (int k = 0; k < 2; ++k) \
;         acc[ai][bj][m][n] = __builtin_amdgcn_mfma_f32_16x16x32_bf16(Bt[n][k], At[m][k], acc[ai][bj][m][n], 0, 0, 0); __builtin_amdgcn_s_setprio(0); } while (0)
; #define PG8_WAIT_V(n) asm volatile("s_waitcnt vmcnt(" #n ")" ::: "memory")
; #define PG8_WAIT_L(n) asm volatile("s_waitcnt lgkmcnt(" #n ")" ::: "memory")
; #define PG8_BAR __builtin_amdgcn_s_barrier()
; #define PG8_SCHED __builtin_amdgcn_sched_barrier(0)
; template <class Epi, class Sched, bool ALIGN_EPI = false, bool SP2 = false>
; __device__ __forceinline__ void gemm_phase(PG8_LAS unsigned char* lds, const Gemm g, const Sched& S, const Epi& E) {
;     ...
;             PG8_WAIT_V(8); PG8_WAIT_L(0); PG8_BAR; if (cur.half == 0) { PG8_MMA(1, 0, At, B0); PG8_MMA(1, 1, At, B1); } PG8_BAR; PG8_SCHED;
;             PG8_LDB(B0, 1, 0); PG8_LDB(B1, 1, 1); PG8_SCHED; PG8_LDA(At, 1, 0); PG8_STAGE(PG8_SA(0, 1), a2 + hstep, voffA);
;             PG8_WAIT_V(8); PG8_WAIT_L(0); PG8_BAR; PG8_MMA(0, 0, At, B0); PG8_MMA(0, 1, At, B1); PG8_BAR; PG8_SCHED;
.Lpj_ip_2:
	s_waitcnt lgkmcnt(0)
	s_barrier
	s_setprio 1
	s_waitcnt lgkmcnt(0)
	v_mfma_f32_16x16x32_bf16 v[64:67], v[132:135], v[182:185], 0
	v_mfma_f32_16x16x32_bf16 v[60:63], v[140:143], v[182:185], 0
	v_mfma_f32_16x16x32_bf16 v[48:51], v[132:135], v[190:193], 0
	v_mfma_f32_16x16x32_bf16 v[44:47], v[140:143], v[190:193], 0
	v_mfma_f32_16x16x32_bf16 v[32:35], v[132:135], v[198:201], 0
	v_mfma_f32_16x16x32_bf16 v[28:31], v[140:143], v[198:201], 0
	v_mfma_f32_16x16x32_bf16 v[16:19], v[132:135], v[212:215], 0
	v_mfma_f32_16x16x32_bf16 v[12:15], v[140:143], v[212:215], 0
	v_mfma_f32_16x16x32_bf16 v[64:67], v[136:139], v[186:189], v[64:67]
	v_mfma_f32_16x16x32_bf16 v[60:63], v[144:147], v[186:189], v[60:63]
	v_mfma_f32_16x16x32_bf16 v[48:51], v[136:139], v[194:197], v[48:51]
	v_mfma_f32_16x16x32_bf16 v[44:47], v[144:147], v[194:197], v[44:47]
	v_mfma_f32_16x16x32_bf16 v[32:35], v[136:139], v[208:211], v[32:35]
	v_mfma_f32_16x16x32_bf16 v[28:31], v[144:147], v[208:211], v[28:31]
	v_mfma_f32_16x16x32_bf16 v[16:19], v[136:139], v[216:219], v[16:19]
	v_mfma_f32_16x16x32_bf16 v[12:15], v[144:147], v[216:219], v[12:15]
	s_setprio 0
	s_setprio 1
	v_mfma_f32_16x16x32_bf16 v[56:59], v[148:151], v[182:185], 0
	v_mfma_f32_16x16x32_bf16 v[52:55], v[156:159], v[182:185], 0
	v_mfma_f32_16x16x32_bf16 v[40:43], v[148:151], v[190:193], 0
	v_mfma_f32_16x16x32_bf16 v[36:39], v[156:159], v[190:193], 0
	v_mfma_f32_16x16x32_bf16 v[24:27], v[148:151], v[198:201], 0
	v_mfma_f32_16x16x32_bf16 v[20:23], v[156:159], v[198:201], 0
	v_mfma_f32_16x16x32_bf16 v[8:11], v[148:151], v[212:215], 0
	v_mfma_f32_16x16x32_bf16 v[4:7], v[156:159], v[212:215], 0
	v_mfma_f32_16x16x32_bf16 v[56:59], v[152:155], v[186:189], v[56:59]
	v_mfma_f32_16x16x32_bf16 v[52:55], v[160:163], v[186:189], v[52:55]
	v_mfma_f32_16x16x32_bf16 v[40:43], v[152:155], v[194:197], v[40:43]
	v_mfma_f32_16x16x32_bf16 v[36:39], v[160:163], v[194:197], v[36:39]
	v_mfma_f32_16x16x32_bf16 v[24:27], v[152:155], v[208:211], v[24:27]
	v_mfma_f32_16x16x32_bf16 v[20:23], v[160:163], v[208:211], v[20:23]
	v_mfma_f32_16x16x32_bf16 v[8:11], v[152:155], v[216:219], v[8:11]
	v_mfma_f32_16x16x32_bf16 v[4:7], v[160:163], v[216:219], v[4:7]
	s_setprio 0
	s_barrier
	ds_read_b128 v[132:135], v238 offset:32768
	ds_read_b128 v[136:139], v238 offset:33792
	ds_read_b128 v[140:143], v238 offset:34816
	ds_read_b128 v[144:147], v238 offset:35840
	ds_read_b128 v[148:151], v238 offset:49152
	ds_read_b128 v[152:155], v238 offset:50176
	ds_read_b128 v[156:159], v238 offset:51200
	ds_read_b128 v[160:163], v238 offset:52224
	s_add_u32 s10, s10, 0x40000
	s_addc_u32 s11, s11, 0
	s_mov_b32 m0, s31
	ds_read_b128 v[182:185], v206 offset:32768
	ds_read_b128 v[186:189], v206 offset:33792
	ds_read_b128 v[190:193], v206 offset:34816
	ds_read_b128 v[194:197], v206 offset:35840
	global_load_lds_dwordx4 v164, s[10:11]
	s_mov_b32 m0, s34
	ds_read_b128 v[198:201], v206 offset:36864
	ds_read_b128 v[208:211], v206 offset:37888
	ds_read_b128 v[212:215], v206 offset:38912
	ds_read_b128 v[216:219], v206 offset:39936
	global_load_lds_dwordx4 v168, s[10:11]
	s_waitcnt vmcnt(8)
	s_waitcnt lgkmcnt(0)
	s_barrier
	s_setprio 1
	s_waitcnt lgkmcnt(0)
	v_mfma_f32_16x16x32_bf16 v[128:131], v[132:135], v[182:185], v[128:131]
	v_mfma_f32_16x16x32_bf16 v[124:127], v[140:143], v[182:185], v[124:127]
	v_mfma_f32_16x16x32_bf16 v[112:115], v[132:135], v[190:193], v[112:115]
	v_mfma_f32_16x16x32_bf16 v[108:111], v[140:143], v[190:193], v[108:111]
	v_mfma_f32_16x16x32_bf16 v[96:99], v[132:135], v[198:201], v[96:99]
	v_mfma_f32_16x16x32_bf16 v[92:95], v[140:143], v[198:201], v[92:95]
	v_mfma_f32_16x16x32_bf16 v[80:83], v[132:135], v[212:215], v[80:83]
	v_mfma_f32_16x16x32_bf16 v[76:79], v[140:143], v[212:215], v[76:79]
	v_mfma_f32_16x16x32_bf16 v[128:131], v[136:139], v[186:189], v[128:131]
	v_mfma_f32_16x16x32_bf16 v[124:127], v[144:147], v[186:189], v[124:127]
	v_mfma_f32_16x16x32_bf16 v[112:115], v[136:139], v[194:197], v[112:115]
	v_mfma_f32_16x16x32_bf16 v[108:111], v[144:147], v[194:197], v[108:111]
	v_mfma_f32_16x16x32_bf16 v[96:99], v[136:139], v[208:211], v[96:99]
	v_mfma_f32_16x16x32_bf16 v[92:95], v[144:147], v[208:211], v[92:95]
	v_mfma_f32_16x16x32_bf16 v[80:83], v[136:139], v[216:219], v[80:83]
	v_mfma_f32_16x16x32_bf16 v[76:79], v[144:147], v[216:219], v[76:79]
	s_setprio 0
	s_setprio 1
	v_mfma_f32_16x16x32_bf16 v[120:123], v[148:151], v[182:185], v[120:123]
	v_mfma_f32_16x16x32_bf16 v[116:119], v[156:159], v[182:185], v[116:119]
	v_mfma_f32_16x16x32_bf16 v[104:107], v[148:151], v[190:193], v[104:107]
	v_mfma_f32_16x16x32_bf16 v[100:103], v[156:159], v[190:193], v[100:103]
	v_mfma_f32_16x16x32_bf16 v[88:91], v[148:151], v[198:201], v[88:91]
	v_mfma_f32_16x16x32_bf16 v[84:87], v[156:159], v[198:201], v[84:87]
	v_mfma_f32_16x16x32_bf16 v[72:75], v[148:151], v[212:215], v[72:75]
	v_mfma_f32_16x16x32_bf16 v[68:71], v[156:159], v[212:215], v[68:71]
	v_mfma_f32_16x16x32_bf16 v[120:123], v[152:155], v[186:189], v[120:123]
	v_mfma_f32_16x16x32_bf16 v[116:119], v[160:163], v[186:189], v[116:119]
	v_mfma_f32_16x16x32_bf16 v[104:107], v[152:155], v[194:197], v[104:107]
	v_mfma_f32_16x16x32_bf16 v[100:103], v[160:163], v[194:197], v[100:103]
	v_mfma_f32_16x16x32_bf16 v[88:91], v[152:155], v[208:211], v[88:91]
	v_mfma_f32_16x16x32_bf16 v[84:87], v[160:163], v[208:211], v[84:87]
	v_mfma_f32_16x16x32_bf16 v[72:75], v[152:155], v[216:219], v[72:75]
	v_mfma_f32_16x16x32_bf16 v[68:71], v[160:163], v[216:219], v[68:71]
	s_setprio 0
	s_barrier
; #define PG8_STAGE(bufoff, gbase, voff) do { _Pragma("unroll") for (int _i = 0; _i < 2; ++_i) \
;         __builtin_amdgcn_global_load_lds((const unsigned*)((const char*)(gbase) + (voff)[_i]), (PG8_LAS unsigned*)(lds + (bufoff) + ldsw + _i * 8192), 16, 0, 0); } while (0)
; #define PG8_LDA(dst, b, h) do { _Pragma("unroll") for (int m = 0; m < 4; ++m) _Pragma("unroll") for (int k = 0; k < 2; ++k) dst[m][k] = *(const PG8_LAS bf16x8*)(lds + PG8_SA(b, h) + aoff + m * 2048 + k * 1024); } while (0)
; #define PG8_LDB(dst, b, h) do { _Pragma("unroll") for (int n = 0; n < 2; ++n) _Pragma("unroll") for (int k = 0; k < 2; ++k) dst[n][k] = *(const PG8_LAS bf16x8*)(lds + PG8_SB(b, h) + boff + n * 2048 + k * 1024); } while (0)
; #define PG8_MMA(ai, bj, At, Bt) do { __builtin_amdgcn_s_setprio(1); _Pragma("unroll") for (int m = 0; m < 4; ++m) _Pragma("unroll") for (int n = 0; n < 2; ++n) _Pragma("unroll") for (int k = 0; k < 2; ++k) \
;         acc[ai][bj][m][n] = __builtin_amdgcn_mfma_f32_16x16x32_bf16(Bt[n][k], At[m][k], acc[ai][bj][m][n], 0, 0, 0); __builtin_amdgcn_s_setprio(0); } while (0)
; #define PG8_WAIT_V(n) asm volatile("s_waitcnt vmcnt(" #n ")" ::: "memory")
; #define PG8_WAIT_L(n) asm volatile("s_waitcnt lgkmcnt(" #n ")" ::: "memory")
; #define PG8_BAR __builtin_amdgcn_s_barrier()
; #define PG8_SCHED __builtin_amdgcn_sched_barrier(0)
; template <class Epi, class Sched, bool ALIGN_EPI = false, bool SP2 = false>
; __device__ __forceinline__ void gemm_phase(PG8_LAS unsigned char* lds, const Gemm g, const Sched& S, const Epi& E) {
;     ...
;             PG8_LDB(B0, 0, 0); PG8_LDB(B1, 0, 1); PG8_SCHED; PG8_LDA(At, 0, 0); PG8_STAGE(PG8_SA(1, 1), a1 + hstep, voffA);
;     ...
;             if (PROBE_KIND == 18 && t == 0 && ui > 0 && g.probe) { const unsigned long long tq_ = __builtin_amdgcn_s_memrealtime(); PG8_WAIT_V(8); pg8_probe_acc += (unsigned)(__builtin_amdgcn_s_memrealtime() - tq_); }
;     ...
;             PG8_WAIT_V(8); PG8_WAIT_L(0); PG8_BAR; PG8_MMA(0, 0, At, B0); PG8_MMA(0, 1, At, B1); PG8_BAR; PG8_SCHED;
;     ...
;             PG8_LDA(At, 1, 1); PG8_STAGE(PG8_SB(1, 0), b3, voffB); PG8_STAGE(PG8_SB(1, 1), b3 + hstep, voffB); PG8_STAGE(PG8_SA(1, 0), a3, voffA);
;             PG8_WAIT_V(8); PG8_WAIT_L(0); PG8_BAR; if (cur.half == 0) { PG8_MMA(1, 0, At, B0); PG8_MMA(1, 1, At, B1); } PG8_BAR; PG8_SCHED;
	s_add_u32 s0, s0, 0x80
	s_addc_u32 s1, s1, 0
	s_add_i32 m0, s19, 0x18000
	ds_read_b128 v[182:185], v206 offset:49152
	ds_read_b128 v[186:189], v206 offset:50176
	global_load_lds_dwordx4 v166, s[0:1]
	s_add_i32 m0, s19, 0x1a000
	ds_read_b128 v[190:193], v206 offset:51200
	ds_read_b128 v[194:197], v206 offset:52224
	global_load_lds_dwordx4 v170, s[0:1]
	s_add_u32 s0, s0, 0x40000
	s_addc_u32 s1, s1, 0
	s_add_i32 m0, s19, 0x1c000
	ds_read_b128 v[198:201], v206 offset:53248
	ds_read_b128 v[208:211], v206 offset:54272
	global_load_lds_dwordx4 v166, s[0:1]
	s_add_i32 m0, s19, 0x1e000
	ds_read_b128 v[212:215], v206 offset:55296
	ds_read_b128 v[216:219], v206 offset:56320
	global_load_lds_dwordx4 v170, s[0:1]
	s_sub_u32 s10, s10, 0x3ff80
	s_subb_u32 s11, s11, 0
	s_mov_b32 m0, s41
	s_nop 0
	global_load_lds_dwordx4 v164, s[10:11]
	s_mov_b32 m0, s71
	s_nop 0
	global_load_lds_dwordx4 v168, s[10:11]
	s_waitcnt vmcnt(8)
	s_waitcnt lgkmcnt(0)
	s_barrier
	s_setprio 1
	s_waitcnt lgkmcnt(0)
	v_mfma_f32_16x16x32_bf16 v[64:67], v[132:135], v[182:185], v[64:67]
	v_mfma_f32_16x16x32_bf16 v[60:63], v[140:143], v[182:185], v[60:63]
	v_mfma_f32_16x16x32_bf16 v[48:51], v[132:135], v[190:193], v[48:51]
	v_mfma_f32_16x16x32_bf16 v[44:47], v[140:143], v[190:193], v[44:47]
	v_mfma_f32_16x16x32_bf16 v[32:35], v[132:135], v[198:201], v[32:35]
	v_mfma_f32_16x16x32_bf16 v[28:31], v[140:143], v[198:201], v[28:31]
	v_mfma_f32_16x16x32_bf16 v[16:19], v[132:135], v[212:215], v[16:19]
	v_mfma_f32_16x16x32_bf16 v[12:15], v[140:143], v[212:215], v[12:15]
	v_mfma_f32_16x16x32_bf16 v[64:67], v[136:139], v[186:189], v[64:67]
	v_mfma_f32_16x16x32_bf16 v[60:63], v[144:147], v[186:189], v[60:63]
	v_mfma_f32_16x16x32_bf16 v[48:51], v[136:139], v[194:197], v[48:51]
	v_mfma_f32_16x16x32_bf16 v[44:47], v[144:147], v[194:197], v[44:47]
	v_mfma_f32_16x16x32_bf16 v[32:35], v[136:139], v[208:211], v[32:35]
	v_mfma_f32_16x16x32_bf16 v[28:31], v[144:147], v[208:211], v[28:31]
	v_mfma_f32_16x16x32_bf16 v[16:19], v[136:139], v[216:219], v[16:19]
	v_mfma_f32_16x16x32_bf16 v[12:15], v[144:147], v[216:219], v[12:15]
	s_setprio 0
	s_setprio 1
	v_mfma_f32_16x16x32_bf16 v[56:59], v[148:151], v[182:185], v[56:59]
	v_mfma_f32_16x16x32_bf16 v[52:55], v[156:159], v[182:185], v[52:55]
	v_mfma_f32_16x16x32_bf16 v[40:43], v[148:151], v[190:193], v[40:43]
	v_mfma_f32_16x16x32_bf16 v[36:39], v[156:159], v[190:193], v[36:39]
	v_mfma_f32_16x16x32_bf16 v[24:27], v[148:151], v[198:201], v[24:27]
	v_mfma_f32_16x16x32_bf16 v[20:23], v[156:159], v[198:201], v[20:23]
	v_mfma_f32_16x16x32_bf16 v[8:11], v[148:151], v[212:215], v[8:11]
	v_mfma_f32_16x16x32_bf16 v[4:7], v[156:159], v[212:215], v[4:7]
	v_mfma_f32_16x16x32_bf16 v[56:59], v[152:155], v[186:189], v[56:59]
	v_mfma_f32_16x16x32_bf16 v[52:55], v[160:163], v[186:189], v[52:55]
	v_mfma_f32_16x16x32_bf16 v[40:43], v[152:155], v[194:197], v[40:43]
	v_mfma_f32_16x16x32_bf16 v[36:39], v[160:163], v[194:197], v[36:39]
	v_mfma_f32_16x16x32_bf16 v[24:27], v[152:155], v[208:211], v[24:27]
	v_mfma_f32_16x16x32_bf16 v[20:23], v[160:163], v[208:211], v[20:23]
	v_mfma_f32_16x16x32_bf16 v[8:11], v[152:155], v[216:219], v[8:11]
	v_mfma_f32_16x16x32_bf16 v[4:7], v[160:163], v[216:219], v[4:7]
	s_setprio 0
	s_barrier
	s_add_i32 s39, s39, 2
	s_add_u32 s8, s8, 0x100
	s_addc_u32 s9, s9, 0
	s_add_u32 s36, s36, 0x100
	s_addc_u32 s38, s38, 0
	s_mov_b32 s32, 1
.LBB0_395:
	s_add_u32 s0, s8, 0xfffc0080
	s_addc_u32 s1, s9, -1
	s_cmp_eq_u32 s39, 12
	s_cselect_b32 s11, s12, s1
	s_cselect_b32 s10, s13, s0
	s_cselect_b32 s1, s14, s38
	s_cselect_b32 s0, s15, s36
	ds_read_b128 v[132:135], v238
	ds_read_b128 v[136:139], v238 offset:1024
	ds_read_b128 v[140:143], v238 offset:2048
	ds_read_b128 v[144:147], v238 offset:3072
	ds_read_b128 v[148:151], v238 offset:16384
	ds_read_b128 v[152:155], v238 offset:17408
	ds_read_b128 v[156:159], v238 offset:18432
	ds_read_b128 v[160:163], v238 offset:19456
	s_add_i32 m0, s19, 0xc000
	ds_read_b128 v[182:185], v206
	ds_read_b128 v[186:189], v206 offset:1024
	ds_read_b128 v[190:193], v206 offset:2048
	ds_read_b128 v[194:197], v206 offset:3072
	global_load_lds_dwordx4 v164, s[8:9]
	s_add_i32 m0, s19, 0xe000
	ds_read_b128 v[198:201], v206 offset:4096
	ds_read_b128 v[208:211], v206 offset:5120
	ds_read_b128 v[212:215], v206 offset:6144
	ds_read_b128 v[216:219], v206 offset:7168
	global_load_lds_dwordx4 v168, s[8:9]
	s_waitcnt vmcnt(8)
	s_waitcnt lgkmcnt(0)
	s_barrier
	s_setprio 1
	s_waitcnt lgkmcnt(0)
	v_mfma_f32_16x16x32_bf16 v[128:131], v[132:135], v[182:185], v[128:131]
	v_mfma_f32_16x16x32_bf16 v[124:127], v[140:143], v[182:185], v[124:127]
	v_mfma_f32_16x16x32_bf16 v[112:115], v[132:135], v[190:193], v[112:115]
	v_mfma_f32_16x16x32_bf16 v[108:111], v[140:143], v[190:193], v[108:111]
	v_mfma_f32_16x16x32_bf16 v[96:99], v[132:135], v[198:201], v[96:99]
	v_mfma_f32_16x16x32_bf16 v[92:95], v[140:143], v[198:201], v[92:95]
	v_mfma_f32_16x16x32_bf16 v[80:83], v[132:135], v[212:215], v[80:83]
	v_mfma_f32_16x16x32_bf16 v[76:79], v[140:143], v[212:215], v[76:79]
	v_mfma_f32_16x16x32_bf16 v[128:131], v[136:139], v[186:189], v[128:131]
	v_mfma_f32_16x16x32_bf16 v[124:127], v[144:147], v[186:189], v[124:127]
	v_mfma_f32_16x16x32_bf16 v[112:115], v[136:139], v[194:197], v[112:115]
	v_mfma_f32_16x16x32_bf16 v[108:111], v[144:147], v[194:197], v[108:111]
	v_mfma_f32_16x16x32_bf16 v[96:99], v[136:139], v[208:211], v[96:99]
	v_mfma_f32_16x16x32_bf16 v[92:95], v[144:147], v[208:211], v[92:95]
	v_mfma_f32_16x16x32_bf16 v[80:83], v[136:139], v[216:219], v[80:83]
	v_mfma_f32_16x16x32_bf16 v[76:79], v[144:147], v[216:219], v[76:79]
	s_setprio 0
	s_setprio 1
	v_mfma_f32_16x16x32_bf16 v[120:123], v[148:151], v[182:185], v[120:123]
	v_mfma_f32_16x16x32_bf16 v[116:119], v[156:159], v[182:185], v[116:119]
	v_mfma_f32_16x16x32_bf16 v[104:107], v[148:151], v[190:193], v[104:107]
	v_mfma_f32_16x16x32_bf16 v[100:103], v[156:159], v[190:193], v[100:103]
	v_mfma_f32_16x16x32_bf16 v[88:91], v[148:151], v[198:201], v[88:91]
	v_mfma_f32_16x16x32_bf16 v[84:87], v[156:159], v[198:201], v[84:87]
	v_mfma_f32_16x16x32_bf16 v[72:75], v[148:151], v[212:215], v[72:75]
	v_mfma_f32_16x16x32_bf16 v[68:71], v[156:159], v[212:215], v[68:71]
	v_mfma_f32_16x16x32_bf16 v[120:123], v[152:155], v[186:189], v[120:123]
	v_mfma_f32_16x16x32_bf16 v[116:119], v[160:163], v[186:189], v[116:119]
	v_mfma_f32_16x16x32_bf16 v[104:107], v[152:155], v[194:197], v[104:107]
	v_mfma_f32_16x16x32_bf16 v[100:103], v[160:163], v[194:197], v[100:103]
	v_mfma_f32_16x16x32_bf16 v[88:91], v[152:155], v[208:211], v[88:91]
	v_mfma_f32_16x16x32_bf16 v[84:87], v[160:163], v[208:211], v[84:87]
	v_mfma_f32_16x16x32_bf16 v[72:75], v[152:155], v[216:219], v[72:75]
	v_mfma_f32_16x16x32_bf16 v[68:71], v[160:163], v[216:219], v[68:71]
	s_setprio 0
	s_barrier
; #define PG8_STAGE(bufoff, gbase, voff) do { _Pragma("unroll") for (int _i = 0; _i < 2; ++_i) \
;         __builtin_amdgcn_global_load_lds((const unsigned*)((const char*)(gbase) + (voff)[_i]), (PG8_LAS unsigned*)(lds + (bufoff) + ldsw + _i * 8192), 16, 0, 0); } while (0)
; #define PG8_LDA(dst, b, h) do { _Pragma("unroll") for (int m = 0; m < 4; ++m) _Pragma("unroll") for (int k = 0; k < 2; ++k) dst[m][k] = *(const PG8_LAS bf16x8*)(lds + PG8_SA(b, h) + aoff + m * 2048 + k * 1024); } while (0)
; #define PG8_MMA(ai, bj, At, Bt) do { __builtin_amdgcn_s_setprio(1); _Pragma("unroll") for (int m = 0; m < 4; ++m) _Pragma("unroll") for (int n = 0; n < 2; ++n) _Pragma("unroll") for (int k = 0; k < 2; ++k) \
;         acc[ai][bj][m][n] = __builtin_amdgcn_mfma_f32_16x16x32_bf16(Bt[n][k], At[m][k], acc[ai][bj][m][n], 0, 0, 0); __builtin_amdgcn_s_setprio(0); } while (0)
; #define PG8_WAIT_V(n) asm volatile("s_waitcnt vmcnt(" #n ")" ::: "memory")
; #define PG8_WAIT_L(n) asm volatile("s_waitcnt lgkmcnt(" #n ")" ::: "memory")
; #define PG8_BAR __builtin_amdgcn_s_barrier()
; #define PG8_SCHED __builtin_amdgcn_sched_barrier(0)
; template <class Epi, class Sched, bool ALIGN_EPI = false, bool SP2 = false>
; __device__ __forceinline__ void gemm_phase(PG8_LAS unsigned char* lds, const Gemm g, const Sched& S, const Epi& E) {
;     ...
;             PG8_WAIT_V(8); PG8_WAIT_L(0); PG8_BAR; PG8_MMA(0, 0, At, B0); PG8_MMA(0, 1, At, B1); PG8_BAR; PG8_SCHED;
;             PG8_LDA(At, 0, 1); PG8_STAGE(PG8_SB(0, 0), b2, voffB); PG8_STAGE(PG8_SB(0, 1), b2 + hstep, voffB); PG8_STAGE(PG8_SA(0, 0), a2, voffA);
;             PG8_WAIT_V(8); PG8_WAIT_L(0); PG8_BAR; if (cur.half == 0) { PG8_MMA(1, 0, At, B0); PG8_MMA(1, 1, At, B1); } PG8_BAR; PG8_SCHED;
	s_add_i32 m0, s19, 0x10000
	ds_read_b128 v[182:185], v206 offset:16384
	ds_read_b128 v[186:189], v206 offset:17408
	global_load_lds_dwordx4 v166, s[0:1]
	s_add_i32 m0, s19, 0x12000
	s_add_u32 s78, s0, 0x40000
	s_addc_u32 s79, s1, 0
	ds_read_b128 v[190:193], v206 offset:18432
	ds_read_b128 v[194:197], v206 offset:19456
	global_load_lds_dwordx4 v170, s[0:1]
	s_add_i32 m0, s19, 0x14000
	ds_read_b128 v[198:201], v206 offset:20480
	ds_read_b128 v[208:211], v206 offset:21504
	global_load_lds_dwordx4 v166, s[78:79]
	s_add_i32 m0, s19, 0x16000
	ds_read_b128 v[212:215], v206 offset:22528
	ds_read_b128 v[216:219], v206 offset:23552
	global_load_lds_dwordx4 v170, s[78:79]
	s_mov_b32 m0, s19
	s_nop 0
	global_load_lds_dwordx4 v164, s[10:11]
	s_mov_b32 m0, s30
	s_nop 0
	global_load_lds_dwordx4 v168, s[10:11]
	s_waitcnt vmcnt(8)
	s_waitcnt lgkmcnt(0)
	s_barrier
	s_setprio 1
	s_waitcnt lgkmcnt(0)
	v_mfma_f32_16x16x32_bf16 v[64:67], v[132:135], v[182:185], v[64:67]
	v_mfma_f32_16x16x32_bf16 v[60:63], v[140:143], v[182:185], v[60:63]
	v_mfma_f32_16x16x32_bf16 v[48:51], v[132:135], v[190:193], v[48:51]
	v_mfma_f32_16x16x32_bf16 v[44:47], v[140:143], v[190:193], v[44:47]
	v_mfma_f32_16x16x32_bf16 v[32:35], v[132:135], v[198:201], v[32:35]
	v_mfma_f32_16x16x32_bf16 v[28:31], v[140:143], v[198:201], v[28:31]
	v_mfma_f32_16x16x32_bf16 v[16:19], v[132:135], v[212:215], v[16:19]
	v_mfma_f32_16x16x32_bf16 v[12:15], v[140:143], v[212:215], v[12:15]
	v_mfma_f32_16x16x32_bf16 v[64:67], v[136:139], v[186:189], v[64:67]
	v_mfma_f32_16x16x32_bf16 v[60:63], v[144:147], v[186:189], v[60:63]
	v_mfma_f32_16x16x32_bf16 v[48:51], v[136:139], v[194:197], v[48:51]
	v_mfma_f32_16x16x32_bf16 v[44:47], v[144:147], v[194:197], v[44:47]
	v_mfma_f32_16x16x32_bf16 v[32:35], v[136:139], v[208:211], v[32:35]
	v_mfma_f32_16x16x32_bf16 v[28:31], v[144:147], v[208:211], v[28:31]
	v_mfma_f32_16x16x32_bf16 v[16:19], v[136:139], v[216:219], v[16:19]
	v_mfma_f32_16x16x32_bf16 v[12:15], v[144:147], v[216:219], v[12:15]
	s_setprio 0
	s_setprio 1
	v_mfma_f32_16x16x32_bf16 v[56:59], v[148:151], v[182:185], v[56:59]
	v_mfma_f32_16x16x32_bf16 v[52:55], v[156:159], v[182:185], v[52:55]
	v_mfma_f32_16x16x32_bf16 v[40:43], v[148:151], v[190:193], v[40:43]
	v_mfma_f32_16x16x32_bf16 v[36:39], v[156:159], v[190:193], v[36:39]
	v_mfma_f32_16x16x32_bf16 v[24:27], v[148:151], v[198:201], v[24:27]
	v_mfma_f32_16x16x32_bf16 v[20:23], v[156:159], v[198:201], v[20:23]
	v_mfma_f32_16x16x32_bf16 v[8:11], v[148:151], v[212:215], v[8:11]
	v_mfma_f32_16x16x32_bf16 v[4:7], v[156:159], v[212:215], v[4:7]
	v_mfma_f32_16x16x32_bf16 v[56:59], v[152:155], v[186:189], v[56:59]
	v_mfma_f32_16x16x32_bf16 v[52:55], v[160:163], v[186:189], v[52:55]
	v_mfma_f32_16x16x32_bf16 v[40:43], v[152:155], v[194:197], v[40:43]
	v_mfma_f32_16x16x32_bf16 v[36:39], v[160:163], v[194:197], v[36:39]
	v_mfma_f32_16x16x32_bf16 v[24:27], v[152:155], v[208:211], v[24:27]
	v_mfma_f32_16x16x32_bf16 v[20:23], v[160:163], v[208:211], v[20:23]
	v_mfma_f32_16x16x32_bf16 v[8:11], v[152:155], v[216:219], v[8:11]
	v_mfma_f32_16x16x32_bf16 v[4:7], v[160:163], v[216:219], v[4:7]
	s_setprio 0
	s_barrier
	ds_read_b128 v[132:135], v238 offset:32768
	ds_read_b128 v[136:139], v238 offset:33792
	ds_read_b128 v[140:143], v238 offset:34816
	ds_read_b128 v[144:147], v238 offset:35840
	ds_read_b128 v[148:151], v238 offset:49152
	ds_read_b128 v[152:155], v238 offset:50176
	ds_read_b128 v[156:159], v238 offset:51200
	ds_read_b128 v[160:163], v238 offset:52224
	s_add_u32 s10, s10, 0x40000
	s_addc_u32 s11, s11, 0
	s_mov_b32 m0, s31
	ds_read_b128 v[182:185], v206 offset:32768
	ds_read_b128 v[186:189], v206 offset:33792
	ds_read_b128 v[190:193], v206 offset:34816
	ds_read_b128 v[194:197], v206 offset:35840
	global_load_lds_dwordx4 v164, s[10:11]
	s_mov_b32 m0, s34
	ds_read_b128 v[198:201], v206 offset:36864
	ds_read_b128 v[208:211], v206 offset:37888
	ds_read_b128 v[212:215], v206 offset:38912
	ds_read_b128 v[216:219], v206 offset:39936
	global_load_lds_dwordx4 v168, s[10:11]
	s_waitcnt vmcnt(8)
	s_waitcnt lgkmcnt(0)
	s_barrier
; #define PG8_STAGE(bufoff, gbase, voff) do { _Pragma("unroll") for (int _i = 0; _i < 2; ++_i) \
;         __builtin_amdgcn_global_load_lds((const unsigned*)((const char*)(gbase) + (voff)[_i]), (PG8_LAS unsigned*)(lds + (bufoff) + ldsw + _i * 8192), 16, 0, 0); } while (0)
; #define PG8_LDA(dst, b, h) do { _Pragma("unroll") for (int m = 0; m < 4; ++m) _Pragma("unroll") for (int k = 0; k < 2; ++k) dst[m][k] = *(const PG8_LAS bf16x8*)(lds + PG8_SA(b, h) + aoff + m * 2048 + k * 1024); } while (0)
; #define PG8_LDB(dst, b, h) do { _Pragma("unroll") for (int n = 0; n < 2; ++n) _Pragma("unroll") for (int k = 0; k < 2; ++k) dst[n][k] = *(const PG8_LAS bf16x8*)(lds + PG8_SB(b, h) + boff + n * 2048 + k * 1024); } while (0)
; #define PG8_MMA(ai, bj, At, Bt) do { __builtin_amdgcn_s_setprio(1); _Pragma("unroll") for (int m = 0; m < 4; ++m) _Pragma("unroll") for (int n = 0; n < 2; ++n) _Pragma("unroll") for (int k = 0; k < 2; ++k) \
;         acc[ai][bj][m][n] = __builtin_amdgcn_mfma_f32_16x16x32_bf16(Bt[n][k], At[m][k], acc[ai][bj][m][n], 0, 0, 0); __builtin_amdgcn_s_setprio(0); } while (0)
; #define PG8_WAIT_V(n) asm volatile("s_waitcnt vmcnt(" #n ")" ::: "memory")
; #define PG8_WAIT_L(n) asm volatile("s_waitcnt lgkmcnt(" #n ")" ::: "memory")
; #define PG8_BAR __builtin_amdgcn_s_barrier()
; #define PG8_SCHED __builtin_amdgcn_sched_barrier(0)
; template <class Epi, class Sched, bool ALIGN_EPI = false, bool SP2 = false>
; __device__ __forceinline__ void gemm_phase(PG8_LAS unsigned char* lds, const Gemm g, const Sched& S, const Epi& E) {
;     ...
;             PG8_WAIT_V(8); PG8_WAIT_L(0); PG8_BAR; if (cur.half == 0) { PG8_MMA(1, 0, At, B0); PG8_MMA(1, 1, At, B1); } PG8_BAR; PG8_SCHED;
;             PG8_LDB(B0, 1, 0); PG8_LDB(B1, 1, 1); PG8_SCHED; PG8_LDA(At, 1, 0); PG8_STAGE(PG8_SA(0, 1), a2 + hstep, voffA);
;             PG8_WAIT_V(8); PG8_WAIT_L(0); PG8_BAR; PG8_MMA(0, 0, At, B0); PG8_MMA(0, 1, At, B1); PG8_BAR; PG8_SCHED;
;             PG8_LDA(At, 1, 1); PG8_STAGE(PG8_SB(1, 0), b3, voffB); PG8_STAGE(PG8_SB(1, 1), b3 + hstep, voffB); PG8_STAGE(PG8_SA(1, 0), a3, voffA);
;             PG8_WAIT_V(8); PG8_WAIT_L(0); PG8_BAR; if (cur.half == 0) { PG8_MMA(1, 0, At, B0); PG8_MMA(1, 1, At, B1); } PG8_BAR; PG8_SCHED;
	s_setprio 1
	s_waitcnt lgkmcnt(0)
	v_mfma_f32_16x16x32_bf16 v[128:131], v[132:135], v[182:185], v[128:131]
	v_mfma_f32_16x16x32_bf16 v[124:127], v[140:143], v[182:185], v[124:127]
	v_mfma_f32_16x16x32_bf16 v[112:115], v[132:135], v[190:193], v[112:115]
	v_mfma_f32_16x16x32_bf16 v[108:111], v[140:143], v[190:193], v[108:111]
	v_mfma_f32_16x16x32_bf16 v[96:99], v[132:135], v[198:201], v[96:99]
	v_mfma_f32_16x16x32_bf16 v[92:95], v[140:143], v[198:201], v[92:95]
	v_mfma_f32_16x16x32_bf16 v[80:83], v[132:135], v[212:215], v[80:83]
	v_mfma_f32_16x16x32_bf16 v[76:79], v[140:143], v[212:215], v[76:79]
	v_mfma_f32_16x16x32_bf16 v[128:131], v[136:139], v[186:189], v[128:131]
	v_mfma_f32_16x16x32_bf16 v[124:127], v[144:147], v[186:189], v[124:127]
	v_mfma_f32_16x16x32_bf16 v[112:115], v[136:139], v[194:197], v[112:115]
	v_mfma_f32_16x16x32_bf16 v[108:111], v[144:147], v[194:197], v[108:111]
	v_mfma_f32_16x16x32_bf16 v[96:99], v[136:139], v[208:211], v[96:99]
	v_mfma_f32_16x16x32_bf16 v[92:95], v[144:147], v[208:211], v[92:95]
	v_mfma_f32_16x16x32_bf16 v[80:83], v[136:139], v[216:219], v[80:83]
	v_mfma_f32_16x16x32_bf16 v[76:79], v[144:147], v[216:219], v[76:79]
	s_setprio 0
	s_setprio 1
	v_mfma_f32_16x16x32_bf16 v[120:123], v[148:151], v[182:185], v[120:123]
	v_mfma_f32_16x16x32_bf16 v[116:119], v[156:159], v[182:185], v[116:119]
	v_mfma_f32_16x16x32_bf16 v[104:107], v[148:151], v[190:193], v[104:107]
	v_mfma_f32_16x16x32_bf16 v[100:103], v[156:159], v[190:193], v[100:103]
	v_mfma_f32_16x16x32_bf16 v[88:91], v[148:151], v[198:201], v[88:91]
	v_mfma_f32_16x16x32_bf16 v[84:87], v[156:159], v[198:201], v[84:87]
	v_mfma_f32_16x16x32_bf16 v[72:75], v[148:151], v[212:215], v[72:75]
	v_mfma_f32_16x16x32_bf16 v[68:71], v[156:159], v[212:215], v[68:71]
	v_mfma_f32_16x16x32_bf16 v[120:123], v[152:155], v[186:189], v[120:123]
	v_mfma_f32_16x16x32_bf16 v[116:119], v[160:163], v[186:189], v[116:119]
	v_mfma_f32_16x16x32_bf16 v[104:107], v[152:155], v[194:197], v[104:107]
	v_mfma_f32_16x16x32_bf16 v[100:103], v[160:163], v[194:197], v[100:103]
	v_mfma_f32_16x16x32_bf16 v[88:91], v[152:155], v[208:211], v[88:91]
	v_mfma_f32_16x16x32_bf16 v[84:87], v[160:163], v[208:211], v[84:87]
	v_mfma_f32_16x16x32_bf16 v[72:75], v[152:155], v[216:219], v[72:75]
	v_mfma_f32_16x16x32_bf16 v[68:71], v[160:163], v[216:219], v[68:71]
	s_setprio 0
	s_barrier
	s_add_u32 s0, s0, 0x80
	s_addc_u32 s1, s1, 0
	s_add_i32 m0, s19, 0x18000
	ds_read_b128 v[182:185], v206 offset:49152
	ds_read_b128 v[186:189], v206 offset:50176
	global_load_lds_dwordx4 v166, s[0:1]
	s_add_i32 m0, s19, 0x1a000
	ds_read_b128 v[190:193], v206 offset:51200
	ds_read_b128 v[194:197], v206 offset:52224
	global_load_lds_dwordx4 v170, s[0:1]
	s_add_u32 s0, s0, 0x40000
	s_addc_u32 s1, s1, 0
	s_add_i32 m0, s19, 0x1c000
	ds_read_b128 v[198:201], v206 offset:53248
	ds_read_b128 v[208:211], v206 offset:54272
	global_load_lds_dwordx4 v166, s[0:1]
	s_add_i32 m0, s19, 0x1e000
	ds_read_b128 v[212:215], v206 offset:55296
	ds_read_b128 v[216:219], v206 offset:56320
	global_load_lds_dwordx4 v170, s[0:1]
	s_sub_u32 s10, s10, 0x3ff80
	s_subb_u32 s11, s11, 0
	s_mov_b32 m0, s41
	s_nop 0
	global_load_lds_dwordx4 v164, s[10:11]
	s_mov_b32 m0, s71
	s_nop 0
	global_load_lds_dwordx4 v168, s[10:11]
	s_waitcnt vmcnt(8)
	s_waitcnt lgkmcnt(0)
	s_barrier
	s_setprio 1
	s_waitcnt lgkmcnt(0)
	v_mfma_f32_16x16x32_bf16 v[64:67], v[132:135], v[182:185], v[64:67]
	v_mfma_f32_16x16x32_bf16 v[60:63], v[140:143], v[182:185], v[60:63]
	v_mfma_f32_16x16x32_bf16 v[48:51], v[132:135], v[190:193], v[48:51]
	v_mfma_f32_16x16x32_bf16 v[44:47], v[140:143], v[190:193], v[44:47]
	v_mfma_f32_16x16x32_bf16 v[32:35], v[132:135], v[198:201], v[32:35]
	v_mfma_f32_16x16x32_bf16 v[28:31], v[140:143], v[198:201], v[28:31]
	v_mfma_f32_16x16x32_bf16 v[16:19], v[132:135], v[212:215], v[16:19]
	v_mfma_f32_16x16x32_bf16 v[12:15], v[140:143], v[212:215], v[12:15]
	v_mfma_f32_16x16x32_bf16 v[64:67], v[136:139], v[186:189], v[64:67]
	v_mfma_f32_16x16x32_bf16 v[60:63], v[144:147], v[186:189], v[60:63]
	v_mfma_f32_16x16x32_bf16 v[48:51], v[136:139], v[194:197], v[48:51]
	v_mfma_f32_16x16x32_bf16 v[44:47], v[144:147], v[194:197], v[44:47]
	v_mfma_f32_16x16x32_bf16 v[32:35], v[136:139], v[208:211], v[32:35]
	v_mfma_f32_16x16x32_bf16 v[28:31], v[144:147], v[208:211], v[28:31]
	v_mfma_f32_16x16x32_bf16 v[16:19], v[136:139], v[216:219], v[16:19]
	v_mfma_f32_16x16x32_bf16 v[12:15], v[144:147], v[216:219], v[12:15]
	s_setprio 0
	s_setprio 1
	v_mfma_f32_16x16x32_bf16 v[56:59], v[148:151], v[182:185], v[56:59]
	v_mfma_f32_16x16x32_bf16 v[52:55], v[156:159], v[182:185], v[52:55]
	v_mfma_f32_16x16x32_bf16 v[40:43], v[148:151], v[190:193], v[40:43]
	v_mfma_f32_16x16x32_bf16 v[36:39], v[156:159], v[190:193], v[36:39]
	v_mfma_f32_16x16x32_bf16 v[24:27], v[148:151], v[198:201], v[24:27]
	v_mfma_f32_16x16x32_bf16 v[20:23], v[156:159], v[198:201], v[20:23]
	v_mfma_f32_16x16x32_bf16 v[8:11], v[148:151], v[212:215], v[8:11]
	v_mfma_f32_16x16x32_bf16 v[4:7], v[156:159], v[212:215], v[4:7]
	v_mfma_f32_16x16x32_bf16 v[56:59], v[152:155], v[186:189], v[56:59]
	v_mfma_f32_16x16x32_bf16 v[52:55], v[160:163], v[186:189], v[52:55]
	v_mfma_f32_16x16x32_bf16 v[40:43], v[152:155], v[194:197], v[40:43]
	v_mfma_f32_16x16x32_bf16 v[36:39], v[160:163], v[194:197], v[36:39]
	v_mfma_f32_16x16x32_bf16 v[24:27], v[152:155], v[208:211], v[24:27]
	v_mfma_f32_16x16x32_bf16 v[20:23], v[160:163], v[208:211], v[20:23]
	v_mfma_f32_16x16x32_bf16 v[8:11], v[152:155], v[216:219], v[8:11]
	v_mfma_f32_16x16x32_bf16 v[4:7], v[160:163], v[216:219], v[4:7]
	s_setprio 0
	s_barrier
	s_add_i32 s39, s39, 2
	s_add_u32 s8, s8, 0x100
	s_addc_u32 s9, s9, 0
	s_add_u32 s36, s36, 0x100
	s_addc_u32 s38, s38, 0
	s_cmp_gt_u32 s39, 13
	s_cbranch_scc0 .LBB0_395
	s_and_b64 vcc, exec, s[58:59]
	s_cbranch_vccz .LBB0_398
	s_barrier
